# stack24 = stack23 + neighbourhood attention QK^T: K fragments read 6 ds_reads ahead (d 0-31 fragment straight into the score tile's registers, ring-slot offsets formed at the top)
# baseline (speedup 1.0000x reference)
; DEVINL void phase3(const Params& P, unsigned char* smem) {
;     ...
;             f32x4 sc[16];
;             float mx = -3.0e38f;
; #pragma unroll
;             for (int tt = 0; tt < 16; ++tt) {
;                 const int sl = ((r0 + (tt >> 1)) % 9) * 8192, row = kc0 + (tt & 1) * 16 + lr;
;                 const bf16x8 k0 = *(const bf16x8*)(smem + KR + sl + k_off(row, g)), k1 = *(const bf16x8*)(smem + KR + sl + k_off(row, 4 + g));
;                 f32x4 a = bia[tt];
;                 a = __builtin_amdgcn_mfma_f32_16x16x32_bf16(k0, q0, a, 0, 0, 0);
;                 a = __builtin_amdgcn_mfma_f32_16x16x32_bf16(k1, q1, a, 0, 0, 0);
;                 sc[tt] = a;
;                 if ((tt & 3) == 3) asm volatile("" ::: "memory");
;             }
.LBB0_467:
	s_add_i32 s0, s82, s85
	s_min_u32 s1, s0, 0x7b
	s_min_u32 s48, s0, 0x79
	s_add_i32 s1, s1, 4
	s_cmp_gt_u32 s0, 2
	s_cselect_b32 s65, s1, 7
	s_add_i32 s48, s48, 6
	s_cmp_lg_u32 s0, 0
	s_mul_hi_i32 s1, s30, 0x38e38e39
	s_cselect_b32 s0, s48, 7
	s_lshr_b32 s48, s1, 31
	s_lshr_b32 s1, s1, 1
	s_add_i32 s1, s1, s48
	s_mul_i32 s1, s1, 9
	s_sub_i32 s1, s30, s1
	s_lshl_b32 s92, s1, 13
	s_add_i32 s88, s92, 0x2000
	s_cmp_eq_u32 s88, 0x12000
	s_cselect_b32 s88, 0, s88
	s_add_i32 s91, s88, 0x2000
	s_cmp_eq_u32 s91, 0x12000
	s_cselect_b32 s91, 0, s91
	s_add_i32 s90, s91, 0x2000
	s_cmp_eq_u32 s90, 0x12000
	s_cselect_b32 s90, 0, s90
	s_add_i32 s89, s90, 0x2000
	s_cmp_eq_u32 s89, 0x12000
	s_cselect_b32 s89, 0, s89
	s_add_i32 s87, s89, 0x2000
	s_cmp_eq_u32 s87, 0x12000
	s_cselect_b32 s87, 0, s87
	s_add_i32 s86, s87, 0x2000
	s_cmp_eq_u32 s86, 0x12000
	s_cselect_b32 s86, 0, s86
	s_add_i32 s67, s86, 0x2000
	s_cmp_eq_u32 s67, 0x12000
	s_cselect_b32 s67, 0, s67
	s_waitcnt vmcnt(4)
	v_add3_u32 v174, s92, v218, v217
	ds_read_b128 v[166:169], v174
	ds_read_b128 v[170:173], v174 offset:2048
	v_add3_u32 v199, s92, v219, v217
	ds_read_b128 v[94:97], v199
	ds_read_b128 v[98:101], v199 offset:2048
	v_add3_u32 v174, s88, v218, v217
	ds_read_b128 v[158:161], v174
	ds_read_b128 v[162:165], v174 offset:2048
	v_add3_u32 v199, s88, v219, v217
	ds_read_b128 v[102:105], v199
	s_waitcnt vmcnt(1) lgkmcnt(6)
	v_mfma_f32_16x16x32_bf16 v[166:169], v[166:169], v[90:93], v[22:25]
	s_add_i32 s1, s92, 0
	s_add_i32 s48, s30, 1
	s_mul_hi_i32 s49, s48, 0x38e38e39
	ds_read_b128 v[106:109], v199 offset:2048
	s_waitcnt lgkmcnt(6)
	v_mfma_f32_16x16x32_bf16 v[170:173], v[170:173], v[90:93], v[54:57]
	s_lshr_b32 s52, s49, 31
	s_lshr_b32 s49, s49, 1
	s_add_i32 s49, s49, s52
	v_add3_u32 v174, s91, v218, v217
	ds_read_b128 v[150:153], v174
	s_waitcnt vmcnt(0) lgkmcnt(6)
	v_mfma_f32_16x16x32_bf16 v[166:169], v[94:97], v[86:89], v[166:169]
	s_mul_i32 s49, s49, 9
	s_sub_i32 s48, s48, s49
	s_lshl_b32 s88, s48, 13
	ds_read_b128 v[154:157], v174 offset:2048
	s_waitcnt lgkmcnt(6)
	v_mfma_f32_16x16x32_bf16 v[170:173], v[98:101], v[86:89], v[170:173]
	s_add_i32 s48, s88, 0
	s_add_i32 s49, s30, 2
	s_mul_hi_i32 s52, s49, 0x38e38e39
	v_add3_u32 v199, s91, v219, v217
	ds_read_b128 v[94:97], v199
	s_waitcnt lgkmcnt(6)
	v_mfma_f32_16x16x32_bf16 v[158:161], v[158:161], v[90:93], v[26:29]
	s_lshr_b32 s53, s52, 31
	s_lshr_b32 s52, s52, 1
	s_add_i32 s52, s52, s53
	ds_read_b128 v[98:101], v199 offset:2048
	s_waitcnt lgkmcnt(6)
	v_mfma_f32_16x16x32_bf16 v[162:165], v[162:165], v[90:93], v[58:61]
	s_mul_i32 s52, s52, 9
	s_sub_i32 s49, s49, s52
	s_lshl_b32 s91, s49, 13
	v_add3_u32 v174, s90, v218, v217
	ds_read_b128 v[142:145], v174
	s_waitcnt lgkmcnt(6)
	v_mfma_f32_16x16x32_bf16 v[158:161], v[102:105], v[86:89], v[158:161]
	s_add_i32 s49, s91, 0
	s_add_i32 s1, s30, 3
	s_mul_hi_i32 s52, s1, 0x38e38e39
	ds_read_b128 v[146:149], v174 offset:2048
	s_waitcnt lgkmcnt(6)
	v_mfma_f32_16x16x32_bf16 v[162:165], v[106:109], v[86:89], v[162:165]
	s_lshr_b32 s53, s52, 31
	s_lshr_b32 s52, s52, 1
	s_add_i32 s52, s52, s53
	v_add3_u32 v199, s90, v219, v217
	ds_read_b128 v[102:105], v199
	s_waitcnt lgkmcnt(6)
	v_mfma_f32_16x16x32_bf16 v[150:153], v[150:153], v[90:93], v[30:33]
	s_mul_i32 s52, s52, 9
	s_sub_i32 s1, s1, s52
	s_lshl_b32 s90, s1, 13
	ds_read_b128 v[106:109], v199 offset:2048
	s_waitcnt lgkmcnt(6)
	v_mfma_f32_16x16x32_bf16 v[154:157], v[154:157], v[90:93], v[62:65]
	s_add_i32 s1, s90, 0
	s_add_i32 s48, s30, 4
	s_mul_hi_i32 s52, s48, 0x38e38e39
	v_add3_u32 v174, s89, v218, v217
	ds_read_b128 v[134:137], v174
	s_waitcnt lgkmcnt(6)
	v_mfma_f32_16x16x32_bf16 v[150:153], v[94:97], v[86:89], v[150:153]
	s_lshr_b32 s53, s52, 31
	s_lshr_b32 s49, s52, 1
	s_add_i32 s49, s49, s53
	ds_read_b128 v[138:141], v174 offset:2048
	s_waitcnt lgkmcnt(6)
	v_mfma_f32_16x16x32_bf16 v[154:157], v[98:101], v[86:89], v[154:157]
	s_mul_i32 s49, s49, 9
	s_sub_i32 s48, s48, s49
	s_lshl_b32 s89, s48, 13
	v_add3_u32 v199, s89, v219, v217
	ds_read_b128 v[94:97], v199
	s_waitcnt lgkmcnt(6)
	v_mfma_f32_16x16x32_bf16 v[142:145], v[142:145], v[90:93], v[34:37]
	s_add_i32 s48, s89, 0
	s_add_i32 s1, s30, 5
	s_mul_hi_i32 s49, s1, 0x38e38e39
	ds_read_b128 v[98:101], v199 offset:2048
	s_waitcnt lgkmcnt(6)
	v_mfma_f32_16x16x32_bf16 v[146:149], v[146:149], v[90:93], v[66:69]
	s_lshr_b32 s52, s49, 31
	s_lshr_b32 s49, s49, 1
	s_add_i32 s49, s49, s52
	v_add3_u32 v174, s87, v218, v217
	ds_read_b128 v[126:129], v174
	s_waitcnt lgkmcnt(6)
	v_mfma_f32_16x16x32_bf16 v[142:145], v[102:105], v[86:89], v[142:145]
	s_mul_i32 s49, s49, 9
	s_sub_i32 s1, s1, s49
	s_lshl_b32 s87, s1, 13
	ds_read_b128 v[130:133], v174 offset:2048
	s_waitcnt lgkmcnt(6)
	v_mfma_f32_16x16x32_bf16 v[146:149], v[106:109], v[86:89], v[146:149]
	s_add_i32 s1, s87, 0
	s_add_i32 s48, s30, 6
	s_mul_hi_i32 s49, s48, 0x38e38e39
	v_add3_u32 v199, s87, v219, v217
	ds_read_b128 v[102:105], v199
	s_waitcnt lgkmcnt(6)
; DEVINL void phase3(const Params& P, unsigned char* smem) {
;     ...
;             f32x4 sc[16];
;             float mx = -3.0e38f;
; #pragma unroll
;             for (int tt = 0; tt < 16; ++tt) {
;                 const int sl = ((r0 + (tt >> 1)) % 9) * 8192, row = kc0 + (tt & 1) * 16 + lr;
;                 const bf16x8 k0 = *(const bf16x8*)(smem + KR + sl + k_off(row, g)), k1 = *(const bf16x8*)(smem + KR + sl + k_off(row, 4 + g));
;                 f32x4 a = bia[tt];
;                 a = __builtin_amdgcn_mfma_f32_16x16x32_bf16(k0, q0, a, 0, 0, 0);
;                 a = __builtin_amdgcn_mfma_f32_16x16x32_bf16(k1, q1, a, 0, 0, 0);
;                 sc[tt] = a;
;                 if ((tt & 3) == 3) asm volatile("" ::: "memory");
;             }
;             asm volatile("" ::: "memory");
;             u32x4 kn0, vn0, kn1, vn1;
;             { const int ra = hi_p + 1 <= hi_n ? hi_p + 1 : hi_n, rb = hi_p + 2 <= hi_n ? hi_p + 2 : hi_n;
;               kn0 = *(const u32x4*)(Kg + (size_t)ra * 4096 + t * 8); vn0 = *(const u32x4*)(Vg + (size_t)ra * 4096 + t * 8);
;               kn1 = *(const u32x4*)(Kg + (size_t)rb * 4096 + t * 8); vn1 = *(const u32x4*)(Vg + (size_t)rb * 4096 + t * 8);
;               const bf16_t* qp = Qg + (size_t)((r + (p < 3 ? 2 : 0)) * 64 + c0 + lr) * 64 + 8 * g; qn0 = *(const bf16x8*)qp; qn1 = *(const bf16x8*)(qp + 32); }
;             {
;                 int ma = 0, mb = 0;
; #pragma unroll
;                 for (int tt = 0; tt < 16; ++tt) { ma = imax3(ma, __float_as_int(sc[tt][0]), __float_as_int(sc[tt][1])); mb = imax3(mb, __float_as_int(sc[tt][2]), __float_as_int(sc[tt][3])); }
;                 ma = ma > mb ? ma : mb;
;                 ma = gmaxi4(ma);
;                 if (__builtin_expect(__any(ma == 0), 0)) {
; #pragma unroll
;                     for (int tt = 0; tt < 16; ++tt) mx = fmaxf(fmaxf(mx, fmaxf(sc[tt][0], sc[tt][1])), fmaxf(sc[tt][2], sc[tt][3]));
;                     mx = gmaxf4(mx);
;                 } else mx = __int_as_float(ma);
	v_mfma_f32_16x16x32_bf16 v[134:137], v[134:137], v[90:93], v[38:41]
	s_lshr_b32 s1, s49, 31
	s_lshr_b32 s49, s49, 1
	s_add_i32 s1, s49, s1
	ds_read_b128 v[106:109], v199 offset:2048
	s_waitcnt lgkmcnt(6)
	v_mfma_f32_16x16x32_bf16 v[138:141], v[138:141], v[90:93], v[70:73]
	s_mul_i32 s1, s1, 9
	s_sub_i32 s1, s48, s1
	s_lshl_b32 s86, s1, 13
	v_add3_u32 v174, s86, v218, v217
	ds_read_b128 v[118:121], v174
	s_waitcnt lgkmcnt(6)
	v_mfma_f32_16x16x32_bf16 v[134:137], v[94:97], v[86:89], v[134:137]
	s_add_i32 s1, s86, 0
	s_add_i32 s30, s30, 7
	s_add_i32 s66, s65, 1
	ds_read_b128 v[122:125], v174 offset:2048
	s_waitcnt lgkmcnt(6)
	v_mfma_f32_16x16x32_bf16 v[138:141], v[98:101], v[86:89], v[138:141]
	s_mul_hi_i32 s1, s30, 0x38e38e39
	s_lshr_b32 s48, s1, 31
	s_lshr_b32 s1, s1, 1
	v_add3_u32 v199, s86, v219, v217
	ds_read_b128 v[94:97], v199
	s_waitcnt lgkmcnt(6)
	v_mfma_f32_16x16x32_bf16 v[126:129], v[126:129], v[90:93], v[42:45]
	s_add_i32 s1, s1, s48
	s_mul_i32 s1, s1, 9
	s_sub_i32 s1, s30, s1
	ds_read_b128 v[98:101], v199 offset:2048
	s_waitcnt lgkmcnt(6)
	v_mfma_f32_16x16x32_bf16 v[130:133], v[130:133], v[90:93], v[74:77]
	s_lshl_b32 s67, s1, 13
	s_add_i32 s1, s67, 0
	s_cmp_eq_u32 s85, 6
	v_add3_u32 v174, s67, v218, v217
	ds_read_b128 v[114:117], v174
	s_waitcnt lgkmcnt(6)
	v_mfma_f32_16x16x32_bf16 v[126:129], v[102:105], v[86:89], v[126:129]
	s_cselect_b64 s[48:49], -1, 0
	s_and_b64 s[52:53], s[48:49], exec
	s_cselect_b32 s64, s65, s0
	ds_read_b128 v[110:113], v174 offset:2048
	s_waitcnt lgkmcnt(6)
	v_mfma_f32_16x16x32_bf16 v[130:133], v[106:109], v[86:89], v[130:133]
	s_cselect_b32 s93, 0, 2
	s_cmp_lt_u32 s65, s64
	s_cselect_b64 s[0:1], -1, 0
	v_add3_u32 v199, s67, v219, v217
	ds_read_b128 v[102:105], v199
	s_waitcnt lgkmcnt(6)
	v_mfma_f32_16x16x32_bf16 v[118:121], v[118:121], v[90:93], v[46:49]
	s_and_b64 s[52:53], s[0:1], exec
	s_cselect_b32 s30, s66, s64
	s_add_i32 s65, s65, 2
	ds_read_b128 v[106:109], v199 offset:2048
	s_waitcnt lgkmcnt(6)
	v_mfma_f32_16x16x32_bf16 v[122:125], v[122:125], v[90:93], v[78:81]
	s_min_u32 s52, s65, s64
	s_lshl_b32 s30, s30, 13
	s_waitcnt lgkmcnt(5)
	v_mfma_f32_16x16x32_bf16 v[118:121], v[94:97], v[86:89], v[118:121]
	s_waitcnt lgkmcnt(4)
	v_mfma_f32_16x16x32_bf16 v[122:125], v[98:101], v[86:89], v[122:125]
	s_waitcnt lgkmcnt(3)
	v_mfma_f32_16x16x32_bf16 v[114:117], v[114:117], v[90:93], v[50:53]
	s_waitcnt lgkmcnt(2)
	v_mfma_f32_16x16x32_bf16 v[110:113], v[110:113], v[90:93], v[82:85]
	s_waitcnt lgkmcnt(1)
	v_mfma_f32_16x16x32_bf16 v[114:117], v[102:105], v[86:89], v[114:117]
	s_waitcnt lgkmcnt(0)
	v_mfma_f32_16x16x32_bf16 v[110:113], v[106:109], v[86:89], v[110:113]
	v_max_i32_e32 v199, v168, v169
	v_max3_i32 v199, v199, v172, v173
	v_max3_i32 v199, v199, v160, v161
	v_lshl_add_u64 v[86:87], v[192:193], 0, s[30:31]
	v_lshl_add_u64 v[88:89], v[194:195], 0, s[30:31]
	s_lshl_b32 s30, s52, 13
	global_load_dwordx4 v[106:109], v[86:87], off
	global_load_dwordx4 v[102:105], v[88:89], off
	v_lshl_add_u64 v[86:87], v[192:193], 0, s[30:31]
	v_lshl_add_u64 v[88:89], v[194:195], 0, s[30:31]
	s_add_i32 s30, s83, s93
	s_add_i32 s30, s30, s85
	v_lshl_or_b32 v174, s30, 6, v208
	global_load_dwordx4 v[98:101], v[86:87], off
	global_load_dwordx4 v[94:97], v[88:89], off
	v_lshlrev_b64 v[86:87], 7, v[174:175]
	v_lshl_add_u64 v[86:87], v[190:191], 0, v[86:87]
	global_load_dwordx4 v[90:93], v[86:87], off
	s_nop 0
	global_load_dwordx4 v[86:89], v[86:87], off offset:64
	v_max_i32_e32 v174, v166, v167
	v_max3_i32 v174, v174, v170, v171
	v_max3_i32 v174, v174, v158, v159
	v_max3_i32 v174, v174, v162, v163
	v_max3_i32 v199, v199, v164, v165
	v_max3_i32 v174, v174, v150, v151
	v_max3_i32 v199, v199, v152, v153
	v_max3_i32 v174, v174, v154, v155
	v_max3_i32 v199, v199, v156, v157
	v_max3_i32 v174, v174, v142, v143
	v_max3_i32 v199, v199, v144, v145
	v_max3_i32 v174, v174, v146, v147
	v_max3_i32 v199, v199, v148, v149
	v_max3_i32 v174, v174, v134, v135
	v_max3_i32 v199, v199, v136, v137
	v_max3_i32 v174, v174, v138, v139
	v_max3_i32 v199, v199, v140, v141
	v_max3_i32 v174, v174, v126, v127
	v_max3_i32 v199, v199, v128, v129
	v_max3_i32 v174, v174, v130, v131
	v_max3_i32 v199, v199, v132, v133
	v_max3_i32 v174, v174, v118, v119
	v_max3_i32 v199, v199, v120, v121
	v_max3_i32 v174, v174, v122, v123
	v_max3_i32 v199, v199, v124, v125
	v_max3_i32 v174, v174, v114, v115
	v_max3_i32 v199, v199, v116, v117
	v_max3_i32 v174, v174, v110, v111
	v_max3_i32 v199, v199, v112, v113
	v_max3_i32 v174, v199, v174, 0
	v_mov_b32_e32 v199, v174
	s_nop 1
	v_permlane16_swap_b32_e32 v174, v199
	v_max_i32_e32 v174, v174, v199
	v_mov_b32_e32 v199, v174
	s_nop 1
	v_permlane32_swap_b32_e32 v174, v199
	v_max_i32_e32 v199, v174, v199
	v_cmp_eq_u32_e32 vcc, 0, v199
	s_cbranch_vccnz .LBB0_479
